# GEMM_A quant epilogue: scale stored from lanes 0..15 only (exec-masked, 64 B instead of 256 B per row-group)
# speedup vs baseline: 1.0040x; 1.0040x over previous
LgAq_loop:
	s_waitcnt vmcnt(8) lgkmcnt(0)
	s_barrier
	v_mfma_f32_16x16x32_f16 v[64:67], a[0:3], v[192:195], v[32:35]
	v_mfma_f32_16x16x32_f16 v[68:71], a[4:7], v[192:195], v[36:39]
	v_add_u32_e32 v5, s29, v4
	v_xor_b32_e32 v6, 64, v5
	s_add_u32 s29, s29, 0x4000
	s_cmp_ge_u32 s29, 0x14000
	s_cselect_b32 s29, 0, s29
	v_mfma_f32_16x16x32_f16 v[72:75], a[8:11], v[192:195], v[40:43]
	ds_read_b128 v[128:131], v5 offset:0
	v_mfma_f32_16x16x32_f16 v[76:79], a[12:15], v[192:195], v[44:47]
	ds_read_b128 v[132:135], v6 offset:0
	v_max3_f32 v16, |v48|, 0, |v49|
	v_mfma_f32_16x16x32_f16 v[64:67], a[16:19], v[196:199], v[64:67]
	ds_read_b128 v[136:139], v5 offset:2048
	v_max3_f32 v16, v16, |v50|, |v51|
	v_mfma_f32_16x16x32_f16 v[68:71], a[20:23], v[196:199], v[68:71]
	ds_read_b128 v[140:143], v6 offset:2048
	v_max3_f32 v16, v16, |v52|, |v53|
	v_mfma_f32_16x16x32_f16 v[72:75], a[24:27], v[196:199], v[72:75]
	ds_read_b128 v[144:147], v5 offset:4096
	v_max3_f32 v16, v16, |v54|, |v55|
	v_mfma_f32_16x16x32_f16 v[76:79], a[28:31], v[196:199], v[76:79]
	ds_read_b128 v[148:151], v6 offset:4096
	v_max3_f32 v16, v16, |v56|, |v57|
	v_mfma_f32_16x16x32_f16 v[64:67], a[32:35], v[200:203], v[64:67]
	ds_read_b128 v[152:155], v5 offset:6144
	v_max3_f32 v16, v16, |v58|, |v59|
	v_mfma_f32_16x16x32_f16 v[68:71], a[36:39], v[200:203], v[68:71]
	ds_read_b128 v[156:159], v6 offset:6144
	v_max3_f32 v16, v16, |v60|, |v61|
	v_mfma_f32_16x16x32_f16 v[72:75], a[40:43], v[200:203], v[72:75]
	ds_read_b128 v[160:163], v5 offset:8192
	v_max3_f32 v16, v16, |v62|, |v63|
	v_mfma_f32_16x16x32_f16 v[76:79], a[44:47], v[200:203], v[76:79]
	ds_read_b128 v[164:167], v6 offset:8192
	v_mov_b32_e32 v17, v16
	v_mfma_f32_16x16x32_f16 v[64:67], a[48:51], v[204:207], v[64:67]
	ds_read_b128 v[168:171], v5 offset:10240
	v_mov_b32_e32 v18, v16
	v_mfma_f32_16x16x32_f16 v[68:71], a[52:55], v[204:207], v[68:71]
	ds_read_b128 v[172:175], v6 offset:10240
	v_permlane32_swap_b32_e32 v17, v18
	v_mfma_f32_16x16x32_f16 v[72:75], a[56:59], v[204:207], v[72:75]
	ds_read_b128 v[176:179], v5 offset:12288
	v_max_f32_e32 v16, v17, v18
	v_mfma_f32_16x16x32_f16 v[76:79], a[60:63], v[204:207], v[76:79]
	ds_read_b128 v[180:183], v6 offset:12288
	v_mov_b32_e32 v17, v16
	v_mfma_f32_16x16x32_f16 v[64:67], a[64:67], v[208:211], v[64:67]
	ds_read_b128 v[184:187], v5 offset:14336
	v_mfma_f32_16x16x32_f16 v[68:71], a[68:71], v[208:211], v[68:71]
	ds_read_b128 v[188:191], v6 offset:14336
	v_mov_b32_e32 v18, v16
	v_mfma_f32_16x16x32_f16 v[72:75], a[72:75], v[208:211], v[72:75]
	s_nop 0
	v_permlane16_swap_b32_e32 v17, v18
	v_mfma_f32_16x16x32_f16 v[76:79], a[76:79], v[208:211], v[76:79]
	v_max_f32_e32 v16, v17, v18
	v_mfma_f32_16x16x32_f16 v[64:67], a[80:83], v[212:215], v[64:67]
	v_rcp_f32_e32 v19, v16
	v_mfma_f32_16x16x32_f16 v[68:71], a[84:87], v[212:215], v[68:71]
	v_cmp_lt_f32_e32 vcc, 0, v16
	v_mfma_f32_16x16x32_f16 v[72:75], a[88:91], v[212:215], v[72:75]
	s_mov_b32 m0, s28
	s_add_u32 s28, s28, 0x4000
	s_cmp_ge_u32 s28, s46
	s_cselect_b32 s28, s47, s28
	global_load_lds_dwordx4 v9, s[26:27]
	v_mul_f32_e32 v19, 0x42fe0000, v19
	v_mfma_f32_16x16x32_f16 v[76:79], a[92:95], v[212:215], v[76:79]
	v_mul_f32_e32 v20, 0x3c010204, v16
	v_mfma_f32_16x16x32_f16 v[64:67], a[96:99], v[216:219], v[64:67]
	v_cndmask_b32_e32 v19, 0, v19, vcc
	v_mfma_f32_16x16x32_f16 v[68:71], a[100:103], v[216:219], v[68:71]
	v_cndmask_b32_e32 v20, 1.0, v20, vcc
	v_mfma_f32_16x16x32_f16 v[72:75], a[104:107], v[216:219], v[72:75]
	v_fmaak_f32 v96, v19, v48, 0x4b400000
	v_mfma_f32_16x16x32_f16 v[76:79], a[108:111], v[216:219], v[76:79]
	v_fmaak_f32 v97, v19, v49, 0x4b400000
	v_mfma_f32_16x16x32_f16 v[64:67], a[112:115], v[220:223], v[64:67]
	v_fmaak_f32 v98, v19, v50, 0x4b400000
	v_mfma_f32_16x16x32_f16 v[68:71], a[116:119], v[220:223], v[68:71]
	v_fmaak_f32 v99, v19, v51, 0x4b400000
	v_mfma_f32_16x16x32_f16 v[72:75], a[120:123], v[220:223], v[72:75]
	v_mfma_f32_16x16x32_f16 v[76:79], a[124:127], v[220:223], v[76:79]
	v_fmaak_f32 v100, v19, v52, 0x4b400000
	v_mfma_f32_16x16x32_f16 v[64:67], a[128:131], v[224:227], v[64:67]
	v_fmaak_f32 v101, v19, v53, 0x4b400000
	v_mfma_f32_16x16x32_f16 v[68:71], a[132:135], v[224:227], v[68:71]
	global_load_lds_dwordx4 v9, s[26:27] offset:1024
	v_fmaak_f32 v102, v19, v54, 0x4b400000
	v_mfma_f32_16x16x32_f16 v[72:75], a[136:139], v[224:227], v[72:75]
	v_fmaak_f32 v103, v19, v55, 0x4b400000
	v_mfma_f32_16x16x32_f16 v[76:79], a[140:143], v[224:227], v[76:79]
	v_fmaak_f32 v104, v19, v56, 0x4b400000
	v_mfma_f32_16x16x32_f16 v[64:67], a[144:147], v[228:231], v[64:67]
	v_fmaak_f32 v105, v19, v57, 0x4b400000
	v_mfma_f32_16x16x32_f16 v[68:71], a[148:151], v[228:231], v[68:71]
	v_fmaak_f32 v106, v19, v58, 0x4b400000
	v_mfma_f32_16x16x32_f16 v[72:75], a[152:155], v[228:231], v[72:75]
	v_fmaak_f32 v107, v19, v59, 0x4b400000
	v_mfma_f32_16x16x32_f16 v[76:79], a[156:159], v[228:231], v[76:79]
	v_fmaak_f32 v108, v19, v60, 0x4b400000
	v_mfma_f32_16x16x32_f16 v[64:67], a[160:163], v[232:235], v[64:67]
	v_fmaak_f32 v109, v19, v61, 0x4b400000
	v_mfma_f32_16x16x32_f16 v[68:71], a[164:167], v[232:235], v[68:71]
	v_fmaak_f32 v110, v19, v62, 0x4b400000
	v_mfma_f32_16x16x32_f16 v[72:75], a[168:171], v[232:235], v[72:75]
	v_fmaak_f32 v111, v19, v63, 0x4b400000
	v_mfma_f32_16x16x32_f16 v[76:79], a[172:175], v[232:235], v[76:79]
	v_perm_b32 v21, v97, v96, s44
	v_mfma_f32_16x16x32_f16 v[64:67], a[176:179], v[236:239], v[64:67]
	s_add_u32 m0, m0, 0x800
	s_nop 0
	global_load_lds_dwordx4 v10, s[26:27]
	v_mfma_f32_16x16x32_f16 v[68:71], a[180:183], v[236:239], v[68:71]
	v_perm_b32 v22, v99, v98, s44
	v_mfma_f32_16x16x32_f16 v[72:75], a[184:187], v[236:239], v[72:75]
	v_perm_b32 v23, v101, v100, s44
	v_mfma_f32_16x16x32_f16 v[76:79], a[188:191], v[236:239], v[76:79]
	v_perm_b32 v24, v103, v102, s44
	v_mfma_f32_16x16x32_f16 v[64:67], a[192:195], v[240:243], v[64:67]
	v_perm_b32 v25, v105, v104, s44
	v_mfma_f32_16x16x32_f16 v[68:71], a[196:199], v[240:243], v[68:71]
	v_perm_b32 v26, v107, v106, s44
	v_mfma_f32_16x16x32_f16 v[72:75], a[200:203], v[240:243], v[72:75]
	v_perm_b32 v27, v109, v108, s44
	v_mfma_f32_16x16x32_f16 v[76:79], a[204:207], v[240:243], v[76:79]
	v_perm_b32 v28, v111, v110, s44
	v_mfma_f32_16x16x32_f16 v[64:67], a[208:211], v[244:247], v[64:67]
	v_perm_b32 v96, v22, v21, s45
	v_mfma_f32_16x16x32_f16 v[68:71], a[212:215], v[244:247], v[68:71]
	v_perm_b32 v97, v24, v23, s45
	v_mfma_f32_16x16x32_f16 v[72:75], a[216:219], v[244:247], v[72:75]
	v_perm_b32 v98, v26, v25, s45
	v_mfma_f32_16x16x32_f16 v[76:79], a[220:223], v[244:247], v[76:79]
	v_perm_b32 v99, v28, v27, s45
	v_mfma_f32_16x16x32_f16 v[64:67], a[224:227], v[248:251], v[64:67]
	global_load_lds_dwordx4 v10, s[26:27] offset:1024
	global_store_dwordx4 v14, v[96:99], s[30:31]
	v_mfma_f32_16x16x32_f16 v[68:71], a[228:231], v[248:251], v[68:71]
	s_add_u32 s26, s26, 0x800
	s_addc_u32 s27, s27, 0
	s_mov_b64 exec, 0xffff
	global_store_dword v112, v20, s[30:31]
	s_mov_b64 exec, -1
	v_mfma_f32_16x16x32_f16 v[72:75], a[232:235], v[248:251], v[72:75]
	v_mfma_f32_16x16x32_f16 v[76:79], a[236:239], v[248:251], v[76:79]
	s_add_u32 s30, s30, 0x8800
	s_addc_u32 s31, s31, 0
	v_mfma_f32_16x16x32_f16 v[64:67], a[240:243], v[252:255], v[64:67]
	v_mfma_f32_16x16x32_f16 v[68:71], a[244:247], v[252:255], v[68:71]
	v_mfma_f32_16x16x32_f16 v[72:75], a[248:251], v[252:255], v[72:75]
	v_mfma_f32_16x16x32_f16 v[76:79], a[252:255], v[252:255], v[76:79]
	s_sub_u32 s24, s24, 1
	s_cmp_le_u32 s24, 1
	s_cbranch_scc1 LgAq_exitA
	s_waitcnt vmcnt(8) lgkmcnt(0)
	s_barrier
	v_mfma_f32_16x16x32_f16 v[48:51], a[0:3], v[128:131], v[32:35]
	v_mfma_f32_16x16x32_f16 v[52:55], a[4:7], v[128:131], v[36:39]
	v_add_u32_e32 v7, s29, v4
	v_xor_b32_e32 v8, 64, v7
	s_add_u32 s29, s29, 0x4000
	s_cmp_ge_u32 s29, 0x14000
	s_cselect_b32 s29, 0, s29
	v_mfma_f32_16x16x32_f16 v[56:59], a[8:11], v[128:131], v[40:43]
	ds_read_b128 v[192:195], v7 offset:0
	v_mfma_f32_16x16x32_f16 v[60:63], a[12:15], v[128:131], v[44:47]
	ds_read_b128 v[196:199], v8 offset:0
	v_max3_f32 v16, |v64|, 0, |v65|
	v_mfma_f32_16x16x32_f16 v[48:51], a[16:19], v[132:135], v[48:51]
	ds_read_b128 v[200:203], v7 offset:2048
	v_max3_f32 v16, v16, |v66|, |v67|
	v_mfma_f32_16x16x32_f16 v[52:55], a[20:23], v[132:135], v[52:55]
	ds_read_b128 v[204:207], v8 offset:2048
	v_max3_f32 v16, v16, |v68|, |v69|
	v_mfma_f32_16x16x32_f16 v[56:59], a[24:27], v[132:135], v[56:59]
	ds_read_b128 v[208:211], v7 offset:4096
	v_max3_f32 v16, v16, |v70|, |v71|
	v_mfma_f32_16x16x32_f16 v[60:63], a[28:31], v[132:135], v[60:63]
	ds_read_b128 v[212:215], v8 offset:4096
	v_max3_f32 v16, v16, |v72|, |v73|
	v_mfma_f32_16x16x32_f16 v[48:51], a[32:35], v[136:139], v[48:51]
	ds_read_b128 v[216:219], v7 offset:6144
	v_max3_f32 v16, v16, |v74|, |v75|
	v_mfma_f32_16x16x32_f16 v[52:55], a[36:39], v[136:139], v[52:55]
	ds_read_b128 v[220:223], v8 offset:6144
	v_max3_f32 v16, v16, |v76|, |v77|
	v_mfma_f32_16x16x32_f16 v[56:59], a[40:43], v[136:139], v[56:59]
	ds_read_b128 v[224:227], v7 offset:8192
	v_max3_f32 v16, v16, |v78|, |v79|
	v_mfma_f32_16x16x32_f16 v[60:63], a[44:47], v[136:139], v[60:63]
	ds_read_b128 v[228:231], v8 offset:8192
	v_mov_b32_e32 v17, v16
	v_mfma_f32_16x16x32_f16 v[48:51], a[48:51], v[140:143], v[48:51]
	ds_read_b128 v[232:235], v7 offset:10240
	v_mov_b32_e32 v18, v16
	v_mfma_f32_16x16x32_f16 v[52:55], a[52:55], v[140:143], v[52:55]
	ds_read_b128 v[236:239], v8 offset:10240
	v_permlane32_swap_b32_e32 v17, v18
	v_mfma_f32_16x16x32_f16 v[56:59], a[56:59], v[140:143], v[56:59]
	ds_read_b128 v[240:243], v7 offset:12288
	v_max_f32_e32 v16, v17, v18
	v_mfma_f32_16x16x32_f16 v[60:63], a[60:63], v[140:143], v[60:63]
	ds_read_b128 v[244:247], v8 offset:12288
	v_mov_b32_e32 v17, v16
	v_mfma_f32_16x16x32_f16 v[48:51], a[64:67], v[144:147], v[48:51]
	ds_read_b128 v[248:251], v7 offset:14336
	v_mfma_f32_16x16x32_f16 v[52:55], a[68:71], v[144:147], v[52:55]
	ds_read_b128 v[252:255], v8 offset:14336
	v_mov_b32_e32 v18, v16
	v_mfma_f32_16x16x32_f16 v[56:59], a[72:75], v[144:147], v[56:59]
	s_nop 0
	v_permlane16_swap_b32_e32 v17, v18
	v_mfma_f32_16x16x32_f16 v[60:63], a[76:79], v[144:147], v[60:63]
	v_max_f32_e32 v16, v17, v18
	v_mfma_f32_16x16x32_f16 v[48:51], a[80:83], v[148:151], v[48:51]
	v_rcp_f32_e32 v19, v16
	v_mfma_f32_16x16x32_f16 v[52:55], a[84:87], v[148:151], v[52:55]
	v_cmp_lt_f32_e32 vcc, 0, v16
	v_mfma_f32_16x16x32_f16 v[56:59], a[88:91], v[148:151], v[56:59]
	s_mov_b32 m0, s28
	s_add_u32 s28, s28, 0x4000
	s_cmp_ge_u32 s28, s46
	s_cselect_b32 s28, s47, s28
	global_load_lds_dwordx4 v9, s[26:27]
	v_mul_f32_e32 v19, 0x42fe0000, v19
	v_mfma_f32_16x16x32_f16 v[60:63], a[92:95], v[148:151], v[60:63]
	v_mul_f32_e32 v20, 0x3c010204, v16
	v_mfma_f32_16x16x32_f16 v[48:51], a[96:99], v[152:155], v[48:51]
	v_cndmask_b32_e32 v19, 0, v19, vcc
	v_mfma_f32_16x16x32_f16 v[52:55], a[100:103], v[152:155], v[52:55]
	v_cndmask_b32_e32 v20, 1.0, v20, vcc
	v_mfma_f32_16x16x32_f16 v[56:59], a[104:107], v[152:155], v[56:59]
	v_fmaak_f32 v96, v19, v64, 0x4b400000
	v_mfma_f32_16x16x32_f16 v[60:63], a[108:111], v[152:155], v[60:63]
	v_fmaak_f32 v97, v19, v65, 0x4b400000
	v_mfma_f32_16x16x32_f16 v[48:51], a[112:115], v[156:159], v[48:51]
	v_fmaak_f32 v98, v19, v66, 0x4b400000
	v_mfma_f32_16x16x32_f16 v[52:55], a[116:119], v[156:159], v[52:55]
	v_fmaak_f32 v99, v19, v67, 0x4b400000
	v_mfma_f32_16x16x32_f16 v[56:59], a[120:123], v[156:159], v[56:59]
	v_mfma_f32_16x16x32_f16 v[60:63], a[124:127], v[156:159], v[60:63]
	v_fmaak_f32 v100, v19, v68, 0x4b400000
	v_mfma_f32_16x16x32_f16 v[48:51], a[128:131], v[160:163], v[48:51]
	v_fmaak_f32 v101, v19, v69, 0x4b400000
	v_mfma_f32_16x16x32_f16 v[52:55], a[132:135], v[160:163], v[52:55]
	global_load_lds_dwordx4 v9, s[26:27] offset:1024
	v_fmaak_f32 v102, v19, v70, 0x4b400000
	v_mfma_f32_16x16x32_f16 v[56:59], a[136:139], v[160:163], v[56:59]
	v_fmaak_f32 v103, v19, v71, 0x4b400000
	v_mfma_f32_16x16x32_f16 v[60:63], a[140:143], v[160:163], v[60:63]
	v_fmaak_f32 v104, v19, v72, 0x4b400000
	v_mfma_f32_16x16x32_f16 v[48:51], a[144:147], v[164:167], v[48:51]
	v_fmaak_f32 v105, v19, v73, 0x4b400000
	v_mfma_f32_16x16x32_f16 v[52:55], a[148:151], v[164:167], v[52:55]
	v_fmaak_f32 v106, v19, v74, 0x4b400000
	v_mfma_f32_16x16x32_f16 v[56:59], a[152:155], v[164:167], v[56:59]
	v_fmaak_f32 v107, v19, v75, 0x4b400000
	v_mfma_f32_16x16x32_f16 v[60:63], a[156:159], v[164:167], v[60:63]
	v_fmaak_f32 v108, v19, v76, 0x4b400000
	v_mfma_f32_16x16x32_f16 v[48:51], a[160:163], v[168:171], v[48:51]
	v_fmaak_f32 v109, v19, v77, 0x4b400000
	v_mfma_f32_16x16x32_f16 v[52:55], a[164:167], v[168:171], v[52:55]
	v_fmaak_f32 v110, v19, v78, 0x4b400000
	v_mfma_f32_16x16x32_f16 v[56:59], a[168:171], v[168:171], v[56:59]
	v_fmaak_f32 v111, v19, v79, 0x4b400000
	v_mfma_f32_16x16x32_f16 v[60:63], a[172:175], v[168:171], v[60:63]
	v_perm_b32 v21, v97, v96, s44
	v_mfma_f32_16x16x32_f16 v[48:51], a[176:179], v[172:175], v[48:51]
	s_add_u32 m0, m0, 0x800
	s_nop 0
	global_load_lds_dwordx4 v10, s[26:27]
	v_mfma_f32_16x16x32_f16 v[52:55], a[180:183], v[172:175], v[52:55]
	v_perm_b32 v22, v99, v98, s44
	v_mfma_f32_16x16x32_f16 v[56:59], a[184:187], v[172:175], v[56:59]
	v_perm_b32 v23, v101, v100, s44
	v_mfma_f32_16x16x32_f16 v[60:63], a[188:191], v[172:175], v[60:63]
	v_perm_b32 v24, v103, v102, s44
	v_mfma_f32_16x16x32_f16 v[48:51], a[192:195], v[176:179], v[48:51]
	v_perm_b32 v25, v105, v104, s44
	v_mfma_f32_16x16x32_f16 v[52:55], a[196:199], v[176:179], v[52:55]
	v_perm_b32 v26, v107, v106, s44
	v_mfma_f32_16x16x32_f16 v[56:59], a[200:203], v[176:179], v[56:59]
	v_perm_b32 v27, v109, v108, s44
	v_mfma_f32_16x16x32_f16 v[60:63], a[204:207], v[176:179], v[60:63]
	v_perm_b32 v28, v111, v110, s44
	v_mfma_f32_16x16x32_f16 v[48:51], a[208:211], v[180:183], v[48:51]
	v_perm_b32 v96, v22, v21, s45
	v_mfma_f32_16x16x32_f16 v[52:55], a[212:215], v[180:183], v[52:55]
	v_perm_b32 v97, v24, v23, s45
	v_mfma_f32_16x16x32_f16 v[56:59], a[216:219], v[180:183], v[56:59]
	v_perm_b32 v98, v26, v25, s45
	v_mfma_f32_16x16x32_f16 v[60:63], a[220:223], v[180:183], v[60:63]
	v_perm_b32 v99, v28, v27, s45
	v_mfma_f32_16x16x32_f16 v[48:51], a[224:227], v[184:187], v[48:51]
	global_load_lds_dwordx4 v10, s[26:27] offset:1024
	global_store_dwordx4 v14, v[96:99], s[30:31]
	v_mfma_f32_16x16x32_f16 v[52:55], a[228:231], v[184:187], v[52:55]
	s_add_u32 s26, s26, 0x800
	s_addc_u32 s27, s27, 0
	s_mov_b64 exec, 0xffff
	global_store_dword v112, v20, s[30:31]
	s_mov_b64 exec, -1
	v_mfma_f32_16x16x32_f16 v[56:59], a[232:235], v[184:187], v[56:59]
	v_mfma_f32_16x16x32_f16 v[60:63], a[236:239], v[184:187], v[60:63]
	s_add_u32 s30, s30, 0x8800
	s_addc_u32 s31, s31, 0
	v_mfma_f32_16x16x32_f16 v[48:51], a[240:243], v[188:191], v[48:51]
	v_mfma_f32_16x16x32_f16 v[52:55], a[244:247], v[188:191], v[52:55]
	v_mfma_f32_16x16x32_f16 v[56:59], a[248:251], v[188:191], v[56:59]
	v_mfma_f32_16x16x32_f16 v[60:63], a[252:255], v[188:191], v[60:63]
	s_sub_u32 s24, s24, 1
	s_cmp_le_u32 s24, 1
	s_cbranch_scc0 LgAq_loop
	s_nop 7
	s_nop 7
	v_max3_f32 v16, |v48|, 0, |v49|
	v_max3_f32 v16, v16, |v50|, |v51|
	v_max3_f32 v16, v16, |v52|, |v53|
	v_max3_f32 v16, v16, |v54|, |v55|
	v_max3_f32 v16, v16, |v56|, |v57|
	v_max3_f32 v16, v16, |v58|, |v59|
	v_max3_f32 v16, v16, |v60|, |v61|
	v_max3_f32 v16, v16, |v62|, |v63|
	v_mov_b32_e32 v17, v16
	v_mov_b32_e32 v18, v16
	s_nop 1
	v_permlane32_swap_b32_e32 v17, v18
	v_max_f32_e32 v16, v17, v18
	v_mov_b32_e32 v17, v16
	v_mov_b32_e32 v18, v16
	s_nop 1
	v_permlane16_swap_b32_e32 v17, v18
	v_max_f32_e32 v16, v17, v18
	v_rcp_f32_e32 v19, v16
	v_cmp_lt_f32_e32 vcc, 0, v16
	v_mul_f32_e32 v19, 0x42fe0000, v19
	v_mul_f32_e32 v20, 0x3c010204, v16
	v_cndmask_b32_e32 v19, 0, v19, vcc
	v_cndmask_b32_e32 v20, 1.0, v20, vcc
	v_fmaak_f32 v96, v19, v48, 0x4b400000
	v_fmaak_f32 v97, v19, v49, 0x4b400000
	v_fmaak_f32 v98, v19, v50, 0x4b400000
	v_fmaak_f32 v99, v19, v51, 0x4b400000
	v_fmaak_f32 v100, v19, v52, 0x4b400000
	v_fmaak_f32 v101, v19, v53, 0x4b400000
	v_fmaak_f32 v102, v19, v54, 0x4b400000
	v_fmaak_f32 v103, v19, v55, 0x4b400000
	v_fmaak_f32 v104, v19, v56, 0x4b400000
	v_fmaak_f32 v105, v19, v57, 0x4b400000
	v_fmaak_f32 v106, v19, v58, 0x4b400000
	v_fmaak_f32 v107, v19, v59, 0x4b400000
	v_fmaak_f32 v108, v19, v60, 0x4b400000
	v_fmaak_f32 v109, v19, v61, 0x4b400000
	v_fmaak_f32 v110, v19, v62, 0x4b400000
	v_fmaak_f32 v111, v19, v63, 0x4b400000
	v_perm_b32 v21, v97, v96, s44
	v_perm_b32 v22, v99, v98, s44
	v_perm_b32 v23, v101, v100, s44
	v_perm_b32 v24, v103, v102, s44
	v_perm_b32 v25, v105, v104, s44
	v_perm_b32 v26, v107, v106, s44
	v_perm_b32 v27, v109, v108, s44
	v_perm_b32 v28, v111, v110, s44
	v_perm_b32 v96, v22, v21, s45
	v_perm_b32 v97, v24, v23, s45
	v_perm_b32 v98, v26, v25, s45
	v_perm_b32 v99, v28, v27, s45
	global_store_dwordx4 v14, v[96:99], s[30:31]
	s_mov_b64 exec, 0xffff
	global_store_dword v112, v20, s[30:31]
	s_mov_b64 exec, -1
	s_add_u32 s30, s30, 0x8800
	s_addc_u32 s31, s31, 0
	s_endpgm
LgAq_exitA:
	s_nop 7
	s_nop 7
	v_max3_f32 v16, |v64|, 0, |v65|
	v_max3_f32 v16, v16, |v66|, |v67|
	v_max3_f32 v16, v16, |v68|, |v69|
	v_max3_f32 v16, v16, |v70|, |v71|
	v_max3_f32 v16, v16, |v72|, |v73|
	v_max3_f32 v16, v16, |v74|, |v75|
	v_max3_f32 v16, v16, |v76|, |v77|
	v_max3_f32 v16, v16, |v78|, |v79|
	v_mov_b32_e32 v17, v16
	v_mov_b32_e32 v18, v16
	s_nop 1
	v_permlane32_swap_b32_e32 v17, v18
	v_max_f32_e32 v16, v17, v18
	v_mov_b32_e32 v17, v16
	v_mov_b32_e32 v18, v16
	s_nop 1
	v_permlane16_swap_b32_e32 v17, v18
	v_max_f32_e32 v16, v17, v18
	v_rcp_f32_e32 v19, v16
	v_cmp_lt_f32_e32 vcc, 0, v16
	v_mul_f32_e32 v19, 0x42fe0000, v19
	v_mul_f32_e32 v20, 0x3c010204, v16
	v_cndmask_b32_e32 v19, 0, v19, vcc
	v_cndmask_b32_e32 v20, 1.0, v20, vcc
	v_fmaak_f32 v96, v19, v64, 0x4b400000
	v_fmaak_f32 v97, v19, v65, 0x4b400000
	v_fmaak_f32 v98, v19, v66, 0x4b400000
	v_fmaak_f32 v99, v19, v67, 0x4b400000
	v_fmaak_f32 v100, v19, v68, 0x4b400000
	v_fmaak_f32 v101, v19, v69, 0x4b400000
	v_fmaak_f32 v102, v19, v70, 0x4b400000
	v_fmaak_f32 v103, v19, v71, 0x4b400000
	v_fmaak_f32 v104, v19, v72, 0x4b400000
	v_fmaak_f32 v105, v19, v73, 0x4b400000
	v_fmaak_f32 v106, v19, v74, 0x4b400000
	v_fmaak_f32 v107, v19, v75, 0x4b400000
	v_fmaak_f32 v108, v19, v76, 0x4b400000
	v_fmaak_f32 v109, v19, v77, 0x4b400000
	v_fmaak_f32 v110, v19, v78, 0x4b400000
	v_fmaak_f32 v111, v19, v79, 0x4b400000
	v_perm_b32 v21, v97, v96, s44
	v_perm_b32 v22, v99, v98, s44
	v_perm_b32 v23, v101, v100, s44
	v_perm_b32 v24, v103, v102, s44
	v_perm_b32 v25, v105, v104, s44
	v_perm_b32 v26, v107, v106, s44
	v_perm_b32 v27, v109, v108, s44
	v_perm_b32 v28, v111, v110, s44
	v_perm_b32 v96, v22, v21, s45
	v_perm_b32 v97, v24, v23, s45
	v_perm_b32 v98, v26, v25, s45
	v_perm_b32 v99, v28, v27, s45
	global_store_dwordx4 v14, v[96:99], s[30:31]
	s_mov_b64 exec, 0xffff
	global_store_dword v112, v20, s[30:31]
	s_mov_b64 exec, -1
	s_add_u32 s30, s30, 0x8800
	s_addc_u32 s31, s31, 0
	s_endpgm
